# weight-copy partition: 3072 more MoE items per layer (vs baseline) moved from the prologue to the forgetting-attention workgroups (all remaining gate items)
# baseline (speedup 1.0000x reference)
.LBB0_16:
	s_mul_i32 s0, s33, 0x4200
	s_add_i32 s0, s0, 0
	v_writelane_b32 v247, s22, 11
	s_cmpk_lg_i32 s3, 0x100
	v_writelane_b32 v247, s0, 13
	s_cselect_b64 s[0:1], -1, 0
	s_cmpk_eq_i32 s3, 0x100
	v_writelane_b32 v247, s0, 14
	s_cselect_b64 s[36:37], -1, 0
	s_mov_b32 s5, 0
	v_writelane_b32 v247, s1, 15
	s_and_b64 s[0:1], s[36:37], exec
	s_cselect_b32 s0, 0x2000, 0
	s_sub_i32 s1, 0x6000, s0
	s_lshl_b32 s14, s1, 1
	s_addk_i32 s14, 0x1700
	s_cmp_ge_i32 s56, s14
	s_movk_i32 s15, 0x6000
	s_waitcnt lgkmcnt(0)
	s_barrier
	s_cbranch_scc1 .LBB0_27
	v_lshlrev_b32_e32 v0, 1, v12
	v_ashrrev_i32_e32 v4, 5, v12
	v_and_b32_e32 v0, 62, v0
	s_movk_i32 s4, 0x104
	v_lshlrev_b32_e32 v2, 2, v0
	v_mul_lo_u32 v3, v4, s4
	v_readlane_b32 s4, v247, 13
	v_cvt_f32_u32_e32 v9, s1
	v_lshlrev_b32_e32 v6, 2, v13
	v_add3_u32 v5, s4, v2, v3
	v_lshlrev_b32_e32 v2, 3, v12
	v_and_b32_e32 v2, 56, v2
	v_mul_u32_u24_e32 v3, 0x104, v2
	v_add3_u32 v6, s4, v3, v6
	v_rcp_iflag_f32_e32 v3, v9
	s_sub_i32 s4, 0, s1
	v_mov_b32_e32 v1, 0
	v_add_u32_e32 v7, 8, v13
	v_mul_f32_e32 v3, 0x4f7ffffe, v3
	v_cvt_u32_f32_e32 v3, v3
	v_add_u32_e32 v8, 16, v13
	v_add_u32_e32 v9, 24, v13
	v_add_u32_e32 v10, 32, v13
	v_readfirstlane_b32 s10, v3
	s_mul_i32 s4, s4, s10
	s_mul_hi_u32 s4, s10, s4
	s_add_i32 s16, s10, s4
	s_lshl_b32 s4, s0, 1
	s_add_i32 s4, s33, s4
	v_readlane_b32 s10, v247, 8
	s_add_i32 s4, s4, s10
	v_add_u32_e32 v11, 40, v13
	v_add_u32_e32 v14, 48, v13
	v_add_u32_e32 v15, 56, v13
	s_sub_i32 s17, 0xd6ff, s4
	s_movk_i32 s18, 0x4000
	s_mov_b32 s19, 0x8000
	s_mov_b32 s20, 0xc000
	s_mov_b32 s21, 0x10000
	s_mov_b32 s22, 0x14000
	s_mov_b32 s23, 0x18000
	s_mov_b32 s24, 0x1c000
	s_mov_b32 s25, 0x20000
	s_mov_b32 s26, 0x24000
	s_mov_b32 s27, 0x28000
	s_mov_b32 s28, 0x2c000
	s_mov_b32 s29, 0x30000
	s_mov_b32 s30, 0x34000
	s_mov_b32 s31, 0x38000
	s_mov_b32 s34, 0x3c000
	s_mov_b32 s35, 0x40000
	s_mov_b32 s38, 0x44000
	s_mov_b32 s39, 0x48000
	s_mov_b32 s40, 0x4c000
	s_mov_b32 s41, 0x50000
	s_mov_b32 s42, 0x54000
	s_mov_b32 s43, 0x58000
	s_mov_b32 s44, 0x5c000
	s_mov_b32 s45, 0x60000
	s_mov_b32 s46, 0x64000
	s_mov_b32 s47, 0x68000
	s_mov_b32 s48, 0x6c000
	s_mov_b32 s49, 0x70000
	s_mov_b32 s50, 0x74000
	s_mov_b32 s51, 0x78000
	s_mov_b32 s52, 0x7c000
	v_add_u32_e32 v16, 0x410, v5
	v_add_u32_e32 v17, 0x618, v5
	v_add_u32_e32 v18, 0x820, v5
	v_add_u32_e32 v19, 0xa28, v5
	v_add_u32_e32 v20, 0xc30, v5
	v_add_u32_e32 v21, 0xe38, v5
	v_add_u32_e32 v22, 0x1040, v5
	v_add_u32_e32 v23, 0x1248, v5
	v_add_u32_e32 v24, 0x1450, v5
	v_add_u32_e32 v25, 0x1658, v5
	v_add_u32_e32 v26, 0x1860, v5
	v_add_u32_e32 v27, 0x1a68, v5
	v_add_u32_e32 v28, 0x1c70, v5
	v_add_u32_e32 v29, 0x1e78, v5
	v_add_u32_e32 v30, 0x2080, v5
	v_add_u32_e32 v31, 0x2288, v5
	v_add_u32_e32 v32, 0x2490, v5
	v_add_u32_e32 v33, 0x2698, v5
	v_add_u32_e32 v34, 0x28a0, v5
	v_add_u32_e32 v35, 0x2aa8, v5
	v_add_u32_e32 v36, 0x2cb0, v5
	v_add_u32_e32 v37, 0x2eb8, v5
	v_add_u32_e32 v38, 0x30c0, v5
	v_add_u32_e32 v39, 0x32c8, v5
	v_add_u32_e32 v40, 0x34d0, v5
	v_add_u32_e32 v41, 0x36d8, v5
	v_add_u32_e32 v42, 0x38e0, v5
	v_add_u32_e32 v43, 0x3ae8, v5
	v_add_u32_e32 v44, 0x3cf0, v5
	v_add_u32_e32 v45, 0x3ef8, v5
	s_mov_b32 s53, 0xe000
	s_movk_i32 s54, 0xb8
	s_movk_i32 s55, 0x2000
	s_mov_b32 s57, 0xa000
	s_mov_b32 s59, 0x12000
	s_mov_b32 s60, 0x16000
	s_mov_b32 s61, 0x1a000
	s_mov_b32 s62, 0x1e000
	s_mov_b32 s63, 0x22000
	s_mov_b32 s64, 0x26000
	s_mov_b32 s65, 0x2a000
	s_mov_b32 s66, 0x2e000
	s_mov_b32 s67, 0x32000
	s_mov_b32 s68, 0x36000
	s_mov_b32 s69, 0x3a000
	s_mov_b32 s70, 0x3e000
	s_mov_b32 s71, 0xb850
	v_lshlrev_b32_e32 v0, 2, v0
	v_lshlrev_b32_e32 v2, 1, v2
	v_add_u32_e32 v46, 0x400, v6
	s_mov_b32 s72, s56
	s_branch .LBB0_19

.LBB0_828:
	s_add_i32 s15, s0, 0xc00
	s_ashr_i32 s14, s15, 31
	s_lshr_b32 s14, s14, 23
	s_add_i32 s16, s15, s14
	s_ashr_i32 s14, s16, 9
	s_and_b32 s16, s16, 0xfe00
	s_sub_i32 s44, s15, s16
	s_ashr_i32 s15, s14, 31
	s_sext_i32_i16 s45, s44
	s_lshl_b64 s[16:17], s[14:15], 23
	s_bfe_u32 s14, s45, 0x5001a
	s_add_i32 s14, s44, s14
	s_sext_i32_i16 s15, s14
	s_and_b32 s14, s14, 0xffe0
	s_ashr_i32 s46, s15, 5
	s_sub_i32 s14, s44, s14
	s_waitcnt lgkmcnt(0)
	s_add_u32 s47, s10, s16
	s_addc_u32 s15, s11, s17
	s_add_u32 s45, s12, s16
	s_addc_u32 s44, s13, s17
	s_lshl_b32 s16, s46, 6
	s_lshl_b32 s17, s46, 7
	s_sext_i32_i16 s14, s14
	s_and_b32 s46, s17, 0xffffff00
	s_and_b32 s48, s16, 64
	s_ashr_i32 s17, s16, 31
	s_lshl_b32 s14, s14, 6
	s_or_b32 s46, s48, s46
	s_lshl_b64 s[16:17], s[16:17], 2
	v_add_u32_e32 v4, s14, v6
	s_add_u32 s16, s47, s16
	v_ashrrev_i32_e32 v5, 31, v4
	s_addc_u32 s17, s15, s17
	v_lshlrev_b64 v[4:5], 12, v[4:5]
	v_lshl_add_u64 v[58:59], s[16:17], 0, v[0:1]
	v_lshl_add_u64 v[4:5], v[58:59], 0, v[4:5]
	v_add_co_u32_e32 v58, vcc, s1, v4
	s_ashr_i32 s15, s14, 31
	s_nop 0
	v_addc_co_u32_e32 v59, vcc, 0, v5, vcc
	v_add_co_u32_e32 v60, vcc, s4, v4
	v_add_u32_e32 v42, s46, v7
	s_nop 0
	v_addc_co_u32_e32 v61, vcc, 0, v5, vcc
	v_add_co_u32_e32 v62, vcc, s5, v4
	s_lshl_b64 s[14:15], s[14:15], 1
	s_nop 0
	v_addc_co_u32_e32 v63, vcc, 0, v5, vcc
	v_add_co_u32_e32 v64, vcc, s6, v4
	v_add_u32_e32 v44, 8, v42
	s_nop 0
	v_addc_co_u32_e32 v65, vcc, 0, v5, vcc
	v_add_co_u32_e32 v66, vcc, s7, v4
	v_add_u32_e32 v46, 16, v42
	s_nop 0
	v_addc_co_u32_e32 v67, vcc, 0, v5, vcc
	v_add_co_u32_e32 v68, vcc, s8, v4
	v_add_u32_e32 v48, 24, v42
	s_nop 0
	v_addc_co_u32_e32 v69, vcc, 0, v5, vcc
	v_add_co_u32_e32 v70, vcc, s9, v4
	v_add_u32_e32 v50, 32, v42
	s_nop 0
	v_addc_co_u32_e32 v71, vcc, 0, v5, vcc
	v_add_co_u32_e32 v72, vcc, s18, v4
	v_add_u32_e32 v52, 40, v42
	s_nop 0
	v_addc_co_u32_e32 v73, vcc, 0, v5, vcc
	v_add_co_u32_e32 v74, vcc, s19, v4
	v_add_u32_e32 v54, 48, v42
	s_nop 0
	v_addc_co_u32_e32 v75, vcc, 0, v5, vcc
	v_add_co_u32_e32 v76, vcc, s20, v4
	v_add_u32_e32 v56, 56, v42
	s_nop 0
	v_addc_co_u32_e32 v77, vcc, 0, v5, vcc
	v_add_co_u32_e32 v78, vcc, s21, v4
	s_add_u32 s14, s45, s14
	s_nop 0
	v_addc_co_u32_e32 v79, vcc, 0, v5, vcc
	v_add_co_u32_e32 v80, vcc, s22, v4
	v_ashrrev_i32_e32 v43, 31, v42
	s_nop 0
	v_addc_co_u32_e32 v81, vcc, 0, v5, vcc
	v_add_co_u32_e32 v82, vcc, s23, v4
	v_ashrrev_i32_e32 v45, 31, v44
	s_nop 0
	v_addc_co_u32_e32 v83, vcc, 0, v5, vcc
	v_add_co_u32_e32 v84, vcc, s24, v4
	v_ashrrev_i32_e32 v47, 31, v46
	s_nop 0
	v_addc_co_u32_e32 v85, vcc, 0, v5, vcc
	v_add_co_u32_e32 v86, vcc, s25, v4
	v_ashrrev_i32_e32 v49, 31, v48
	s_nop 0
	v_addc_co_u32_e32 v87, vcc, 0, v5, vcc
	v_add_co_u32_e32 v88, vcc, s26, v4
	v_ashrrev_i32_e32 v51, 31, v50
	s_nop 0
	v_addc_co_u32_e32 v89, vcc, 0, v5, vcc
	v_add_co_u32_e32 v90, vcc, s27, v4
	v_ashrrev_i32_e32 v53, 31, v52
	s_nop 0
	v_addc_co_u32_e32 v91, vcc, 0, v5, vcc
	v_add_co_u32_e32 v92, vcc, s28, v4
	v_ashrrev_i32_e32 v55, 31, v54
	s_nop 0
	v_addc_co_u32_e32 v93, vcc, 0, v5, vcc
	v_add_co_u32_e32 v94, vcc, s29, v4
	v_ashrrev_i32_e32 v57, 31, v56
	s_nop 0
	v_addc_co_u32_e32 v95, vcc, 0, v5, vcc
	v_add_co_u32_e32 v96, vcc, s30, v4
	s_addc_u32 s15, s44, s15
	s_nop 0
	v_addc_co_u32_e32 v97, vcc, 0, v5, vcc
	v_add_co_u32_e32 v98, vcc, s31, v4
	v_lshlrev_b64 v[42:43], 12, v[42:43]
	s_nop 0
	v_addc_co_u32_e32 v99, vcc, 0, v5, vcc
	v_add_co_u32_e32 v100, vcc, s34, v4
	v_lshlrev_b64 v[44:45], 12, v[44:45]
	s_nop 0
	v_addc_co_u32_e32 v101, vcc, 0, v5, vcc
	v_add_co_u32_e32 v102, vcc, s35, v4
	v_lshlrev_b64 v[46:47], 12, v[46:47]
	s_nop 0
	v_addc_co_u32_e32 v103, vcc, 0, v5, vcc
	v_add_co_u32_e32 v104, vcc, s36, v4
	v_lshlrev_b64 v[48:49], 12, v[48:49]
	s_nop 0
	v_addc_co_u32_e32 v105, vcc, 0, v5, vcc
	v_add_co_u32_e32 v106, vcc, s37, v4
	v_lshlrev_b64 v[50:51], 12, v[50:51]
	s_nop 0
	v_addc_co_u32_e32 v107, vcc, 0, v5, vcc
	v_add_co_u32_e32 v108, vcc, s38, v4
	v_lshlrev_b64 v[52:53], 12, v[52:53]
	s_nop 0
	v_addc_co_u32_e32 v109, vcc, 0, v5, vcc
	v_add_co_u32_e32 v110, vcc, s39, v4
	v_lshlrev_b64 v[54:55], 12, v[54:55]
	s_nop 0
	v_addc_co_u32_e32 v111, vcc, 0, v5, vcc
	v_add_co_u32_e32 v112, vcc, s40, v4
	v_lshlrev_b64 v[56:57], 12, v[56:57]
	s_nop 0
	v_addc_co_u32_e32 v113, vcc, 0, v5, vcc
	v_add_co_u32_e32 v114, vcc, s41, v4
	v_lshl_add_u64 v[120:121], s[14:15], 0, v[2:3]
	s_nop 0
	v_addc_co_u32_e32 v115, vcc, 0, v5, vcc
	v_add_co_u32_e32 v116, vcc, s42, v4
	v_lshl_add_u64 v[122:123], v[120:121], 0, v[42:43]
	s_nop 0
	v_addc_co_u32_e32 v117, vcc, 0, v5, vcc
	v_add_co_u32_e32 v118, vcc, s43, v4
	v_lshl_add_u64 v[124:125], v[120:121], 0, v[44:45]
	s_nop 0
	v_addc_co_u32_e32 v119, vcc, 0, v5, vcc
	global_load_dwordx2 v[4:5], v[4:5], off nt
	s_nop 0
	global_load_dwordx2 v[58:59], v[58:59], off nt
	s_nop 0
	global_load_dwordx2 v[60:61], v[60:61], off nt
	s_nop 0
	global_load_dwordx2 v[62:63], v[62:63], off nt
	s_nop 0
	global_load_dwordx2 v[64:65], v[64:65], off nt
	s_nop 0
	global_load_dwordx2 v[66:67], v[66:67], off nt
	s_nop 0
	global_load_dwordx2 v[68:69], v[68:69], off nt
	s_nop 0
	global_load_dwordx2 v[70:71], v[70:71], off nt
	s_nop 0
	global_load_dwordx2 v[72:73], v[72:73], off nt
	s_nop 0
	global_load_dwordx2 v[74:75], v[74:75], off nt
	s_nop 0
	global_load_dwordx2 v[76:77], v[76:77], off nt
	s_nop 0
	global_load_dwordx2 v[78:79], v[78:79], off nt
	s_nop 0
	global_load_dwordx2 v[80:81], v[80:81], off nt
	s_nop 0
	global_load_dwordx2 v[82:83], v[82:83], off nt
	s_nop 0
	global_load_dwordx2 v[84:85], v[84:85], off nt
	s_nop 0
	global_load_dwordx2 v[86:87], v[86:87], off nt
	s_nop 0
	global_load_dwordx2 v[88:89], v[88:89], off nt
	s_nop 0
	global_load_dwordx2 v[90:91], v[90:91], off nt
	s_nop 0
	global_load_dwordx2 v[92:93], v[92:93], off nt
	s_nop 0
	global_load_dwordx2 v[94:95], v[94:95], off nt
	s_nop 0
	global_load_dwordx2 v[96:97], v[96:97], off nt
	s_nop 0
	global_load_dwordx2 v[98:99], v[98:99], off nt
	s_nop 0
	global_load_dwordx2 v[100:101], v[100:101], off nt
	s_nop 0
	global_load_dwordx2 v[102:103], v[102:103], off nt
	s_nop 0
	global_load_dwordx2 v[104:105], v[104:105], off nt
	s_nop 0
	global_load_dwordx2 v[106:107], v[106:107], off nt
	s_nop 0
	global_load_dwordx2 v[108:109], v[108:109], off nt
	s_nop 0
	global_load_dwordx2 v[110:111], v[110:111], off nt
	s_nop 0
	global_load_dwordx2 v[112:113], v[112:113], off nt
	s_nop 0
	global_load_dwordx2 v[114:115], v[114:115], off nt
	s_nop 0
	global_load_dwordx2 v[116:117], v[116:117], off nt
	s_nop 0
	global_load_dwordx2 v[118:119], v[118:119], off nt
	s_waitcnt vmcnt(0)
	ds_write2_b32 v9, v4, v5 offset1:1
	ds_write2_b32 v9, v58, v59 offset0:130 offset1:131
	ds_write2_b32 v10, v60, v61 offset1:1
	ds_write2_b32 v11, v62, v63 offset1:1
	ds_write2_b32 v12, v64, v65 offset1:1
	ds_write2_b32 v13, v66, v67 offset1:1
	ds_write2_b32 v14, v68, v69 offset1:1
	ds_write2_b32 v15, v70, v71 offset1:1
	ds_write2_b32 v16, v72, v73 offset1:1
	ds_write2_b32 v17, v74, v75 offset1:1
	ds_write2_b32 v18, v76, v77 offset1:1
	ds_write2_b32 v19, v78, v79 offset1:1
	ds_write2_b32 v20, v80, v81 offset1:1
	ds_write2_b32 v21, v82, v83 offset1:1
	ds_write2_b32 v22, v84, v85 offset1:1
	ds_write2_b32 v23, v86, v87 offset1:1
	ds_write2_b32 v24, v88, v89 offset1:1
	ds_write2_b32 v25, v90, v91 offset1:1
	ds_write2_b32 v26, v92, v93 offset1:1
	ds_write2_b32 v27, v94, v95 offset1:1
	ds_write2_b32 v28, v96, v97 offset1:1
	ds_write2_b32 v29, v98, v99 offset1:1
	ds_write2_b32 v30, v100, v101 offset1:1
	ds_write2_b32 v31, v102, v103 offset1:1
	ds_write2_b32 v32, v104, v105 offset1:1
	ds_write2_b32 v33, v106, v107 offset1:1
	ds_write2_b32 v34, v108, v109 offset1:1
	ds_write2_b32 v35, v110, v111 offset1:1
	ds_write2_b32 v36, v112, v113 offset1:1
	ds_write2_b32 v37, v114, v115 offset1:1
	ds_write2_b32 v38, v116, v117 offset1:1
	ds_write2_b32 v39, v118, v119 offset1:1
	s_waitcnt lgkmcnt(0)
	v_lshl_add_u64 v[126:127], v[120:121], 0, v[46:47]
	v_lshl_add_u64 v[128:129], v[120:121], 0, v[48:49]
	v_lshl_add_u64 v[130:131], v[120:121], 0, v[50:51]
	v_lshl_add_u64 v[132:133], v[120:121], 0, v[52:53]
	v_lshl_add_u64 v[134:135], v[120:121], 0, v[54:55]
	v_lshl_add_u64 v[120:121], v[120:121], 0, v[56:57]
	ds_read2_b32 v[4:5], v8 offset0:65 offset1:73
	ds_read2_b32 v[46:47], v8 offset1:8
	ds_read2_b32 v[48:49], v8 offset0:130 offset1:138
	ds_read2_b32 v[50:51], v8 offset0:195 offset1:203
	ds_read2_b32 v[52:53], v40 offset0:4 offset1:12
	ds_read2_b32 v[54:55], v40 offset0:69 offset1:77
	ds_read2_b32 v[56:57], v40 offset0:134 offset1:142
	ds_read2_b32 v[58:59], v40 offset0:199 offset1:207
	ds_read2_b32 v[60:61], v8 offset0:81 offset1:89
	ds_read2_b32 v[62:63], v8 offset0:16 offset1:24
	ds_read2_b32 v[64:65], v8 offset0:146 offset1:154
	ds_read2_b32 v[66:67], v8 offset0:211 offset1:219
	ds_read2_b32 v[68:69], v40 offset0:20 offset1:28
	ds_read2_b32 v[70:71], v40 offset0:85 offset1:93
	ds_read2_b32 v[72:73], v40 offset0:150 offset1:158
	ds_read2_b32 v[74:75], v40 offset0:215 offset1:223
	ds_read2_b32 v[76:77], v8 offset0:32 offset1:40
	ds_read2_b32 v[78:79], v8 offset0:97 offset1:105
	ds_read2_b32 v[80:81], v8 offset0:162 offset1:170
	ds_read2_b32 v[82:83], v8 offset0:227 offset1:235
	ds_read2_b32 v[84:85], v40 offset0:36 offset1:44
	ds_read2_b32 v[86:87], v40 offset0:101 offset1:109
	ds_read2_b32 v[88:89], v40 offset0:166 offset1:174
	ds_read2_b32 v[90:91], v40 offset0:231 offset1:239
	ds_read2_b32 v[92:93], v8 offset0:48 offset1:56
	ds_read2_b32 v[94:95], v8 offset0:113 offset1:121
	ds_read2_b32 v[96:97], v8 offset0:178 offset1:186
	ds_read2_b32 v[98:99], v8 offset0:243 offset1:251
	ds_read2_b32 v[100:101], v40 offset0:52 offset1:60
	ds_read2_b32 v[102:103], v40 offset0:117 offset1:125
	ds_read2_b32 v[104:105], v40 offset0:182 offset1:190
	ds_read2_b32 v[106:107], v40 offset0:247 offset1:255
	s_waitcnt lgkmcnt(14)
	v_cvt_pk_bf16_f32 v42, v46, v4
	v_cvt_pk_bf16_f32 v43, v48, v50
	v_cvt_pk_bf16_f32 v44, v52, v54
	v_cvt_pk_bf16_f32 v45, v56, v58
	v_cvt_pk_bf16_f32 v46, v47, v5
	v_cvt_pk_bf16_f32 v47, v49, v51
	v_cvt_pk_bf16_f32 v48, v53, v55
	v_cvt_pk_bf16_f32 v49, v57, v59
	v_cvt_pk_bf16_f32 v50, v62, v60
	v_cvt_pk_bf16_f32 v51, v64, v66
	v_cvt_pk_bf16_f32 v52, v68, v70
	v_cvt_pk_bf16_f32 v53, v72, v74
	v_cvt_pk_bf16_f32 v54, v63, v61
	v_cvt_pk_bf16_f32 v55, v65, v67
	v_cvt_pk_bf16_f32 v56, v69, v71
	v_cvt_pk_bf16_f32 v57, v73, v75
	v_cvt_pk_bf16_f32 v58, v76, v78
	s_waitcnt lgkmcnt(12)
	v_cvt_pk_bf16_f32 v59, v80, v82
	s_waitcnt lgkmcnt(10)
	v_cvt_pk_bf16_f32 v60, v84, v86
	s_waitcnt lgkmcnt(8)
	v_cvt_pk_bf16_f32 v61, v88, v90
	v_cvt_pk_bf16_f32 v62, v77, v79
	v_cvt_pk_bf16_f32 v63, v81, v83
	v_cvt_pk_bf16_f32 v64, v85, v87
	v_cvt_pk_bf16_f32 v65, v89, v91
	s_waitcnt lgkmcnt(6)
	v_cvt_pk_bf16_f32 v66, v92, v94
	s_waitcnt lgkmcnt(4)
	v_cvt_pk_bf16_f32 v67, v96, v98
	s_waitcnt lgkmcnt(2)
	v_cvt_pk_bf16_f32 v68, v100, v102
	s_waitcnt lgkmcnt(0)
	v_cvt_pk_bf16_f32 v69, v104, v106
	v_cvt_pk_bf16_f32 v70, v93, v95
	v_cvt_pk_bf16_f32 v71, v97, v99
	v_cvt_pk_bf16_f32 v72, v101, v103
	v_cvt_pk_bf16_f32 v73, v105, v107
	global_store_dwordx4 v[122:123], v[42:45], off nt
	global_store_dwordx4 v[124:125], v[46:49], off nt
	global_store_dwordx4 v[126:127], v[50:53], off nt
	global_store_dwordx4 v[128:129], v[54:57], off nt
	global_store_dwordx4 v[130:131], v[58:61], off nt
	global_store_dwordx4 v[132:133], v[62:65], off nt
	global_store_dwordx4 v[134:135], v[66:69], off nt
	global_store_dwordx4 v[120:121], v[70:73], off nt
	s_waitcnt lgkmcnt(0)
	s_addk_i32 s0, 0x400
	s_cmpk_gt_i32 s0, 0x13ff
	s_cbranch_scc0 .LBB0_828

.LBB0_2219:
	s_add_i32 s11, s0, 0xc00
	s_ashr_i32 s10, s11, 31
	s_lshr_b32 s10, s10, 23
	s_add_i32 s12, s11, s10
	s_ashr_i32 s10, s12, 9
	s_and_b32 s12, s12, 0xfe00
	s_sub_i32 s12, s11, s12
	s_sext_i32_i16 s13, s12
	s_bfe_u32 s13, s13, 0x5001a
	s_add_i32 s13, s12, s13
	s_ashr_i32 s11, s10, 31
	s_sext_i32_i16 s44, s13
	s_and_b32 s13, s13, 0xffe0
	s_lshl_b64 s[10:11], s[10:11], 23
	s_ashr_i32 s46, s44, 5
	s_sub_i32 s12, s12, s13
	s_add_u32 s10, s10, 0x8000000
	s_sext_i32_i16 s13, s12
	s_addc_u32 s12, s11, 0
	s_waitcnt lgkmcnt(0)
	s_add_u32 s47, s6, s10
	s_addc_u32 s11, s7, s12
	s_add_u32 s45, s8, s10
	s_addc_u32 s44, s9, s12
	s_lshl_b32 s12, s46, 6
	s_lshl_b32 s10, s13, 6
	s_lshl_b32 s13, s46, 7
	s_and_b32 s46, s13, 0xffffff00
	s_and_b32 s48, s12, 64
	s_ashr_i32 s13, s12, 31
	s_or_b32 s46, s48, s46
	s_lshl_b64 s[12:13], s[12:13], 2
	v_add_u32_e32 v4, s10, v74
	s_add_u32 s12, s47, s12
	v_ashrrev_i32_e32 v5, 31, v4
	s_addc_u32 s13, s11, s13
	v_lshlrev_b64 v[4:5], 12, v[4:5]
	v_lshl_add_u64 v[56:57], s[12:13], 0, v[0:1]
	v_lshl_add_u64 v[4:5], v[56:57], 0, v[4:5]
	v_add_co_u32_e32 v56, vcc, s1, v4
	s_ashr_i32 s11, s10, 31
	s_nop 0
	v_addc_co_u32_e32 v57, vcc, 0, v5, vcc
	v_add_co_u32_e32 v58, vcc, s4, v4
	v_add_u32_e32 v40, s46, v75
	s_nop 0
	v_addc_co_u32_e32 v59, vcc, 0, v5, vcc
	v_add_co_u32_e32 v60, vcc, s5, v4
	s_lshl_b64 s[10:11], s[10:11], 1
	s_nop 0
	v_addc_co_u32_e32 v61, vcc, 0, v5, vcc
	v_add_co_u32_e32 v62, vcc, s14, v4
	v_add_u32_e32 v42, 8, v40
	s_nop 0
	v_addc_co_u32_e32 v63, vcc, 0, v5, vcc
	v_add_co_u32_e32 v64, vcc, s15, v4
	v_add_u32_e32 v44, 16, v40
	s_nop 0
	v_addc_co_u32_e32 v65, vcc, 0, v5, vcc
	v_add_co_u32_e32 v66, vcc, s16, v4
	v_add_u32_e32 v46, 24, v40
	s_nop 0
	v_addc_co_u32_e32 v67, vcc, 0, v5, vcc
	v_add_co_u32_e32 v68, vcc, s17, v4
	v_add_u32_e32 v48, 32, v40
	s_nop 0
	v_addc_co_u32_e32 v69, vcc, 0, v5, vcc
	v_add_co_u32_e32 v70, vcc, s18, v4
	v_add_u32_e32 v50, 40, v40
	s_nop 0
	v_addc_co_u32_e32 v71, vcc, 0, v5, vcc
	v_add_co_u32_e32 v72, vcc, s19, v4
	v_add_u32_e32 v52, 48, v40
	s_nop 0
	v_addc_co_u32_e32 v73, vcc, 0, v5, vcc
	v_add_co_u32_e32 v76, vcc, s20, v4
	v_add_u32_e32 v54, 56, v40
	s_nop 0
	v_addc_co_u32_e32 v77, vcc, 0, v5, vcc
	v_add_co_u32_e32 v78, vcc, s21, v4
	s_add_u32 s10, s45, s10
	s_nop 0
	v_addc_co_u32_e32 v79, vcc, 0, v5, vcc
	v_add_co_u32_e32 v80, vcc, s22, v4
	v_ashrrev_i32_e32 v41, 31, v40
	s_nop 0
	v_addc_co_u32_e32 v81, vcc, 0, v5, vcc
	v_add_co_u32_e32 v82, vcc, s23, v4
	v_ashrrev_i32_e32 v43, 31, v42
	s_nop 0
	v_addc_co_u32_e32 v83, vcc, 0, v5, vcc
	v_add_co_u32_e32 v84, vcc, s24, v4
	v_ashrrev_i32_e32 v45, 31, v44
	s_nop 0
	v_addc_co_u32_e32 v85, vcc, 0, v5, vcc
	v_add_co_u32_e32 v86, vcc, s25, v4
	v_ashrrev_i32_e32 v47, 31, v46
	s_nop 0
	v_addc_co_u32_e32 v87, vcc, 0, v5, vcc
	v_add_co_u32_e32 v88, vcc, s26, v4
	v_ashrrev_i32_e32 v49, 31, v48
	s_nop 0
	v_addc_co_u32_e32 v89, vcc, 0, v5, vcc
	v_add_co_u32_e32 v90, vcc, s27, v4
	v_ashrrev_i32_e32 v51, 31, v50
	s_nop 0
	v_addc_co_u32_e32 v91, vcc, 0, v5, vcc
	v_add_co_u32_e32 v92, vcc, s28, v4
	v_ashrrev_i32_e32 v53, 31, v52
	s_nop 0
	v_addc_co_u32_e32 v93, vcc, 0, v5, vcc
	v_add_co_u32_e32 v94, vcc, s29, v4
	v_ashrrev_i32_e32 v55, 31, v54
	s_nop 0
	v_addc_co_u32_e32 v95, vcc, 0, v5, vcc
	v_add_co_u32_e32 v96, vcc, s30, v4
	s_addc_u32 s11, s44, s11
	s_nop 0
	v_addc_co_u32_e32 v97, vcc, 0, v5, vcc
	v_add_co_u32_e32 v98, vcc, s31, v4
	v_lshlrev_b64 v[40:41], 12, v[40:41]
	s_nop 0
	v_addc_co_u32_e32 v99, vcc, 0, v5, vcc
	v_add_co_u32_e32 v100, vcc, s34, v4
	v_lshlrev_b64 v[42:43], 12, v[42:43]
	s_nop 0
	v_addc_co_u32_e32 v101, vcc, 0, v5, vcc
	v_add_co_u32_e32 v102, vcc, s35, v4
	v_lshlrev_b64 v[44:45], 12, v[44:45]
	s_nop 0
	v_addc_co_u32_e32 v103, vcc, 0, v5, vcc
	v_add_co_u32_e32 v104, vcc, s36, v4
	v_lshlrev_b64 v[46:47], 12, v[46:47]
	s_nop 0
	v_addc_co_u32_e32 v105, vcc, 0, v5, vcc
	v_add_co_u32_e32 v106, vcc, s37, v4
	v_lshlrev_b64 v[48:49], 12, v[48:49]
	s_nop 0
	v_addc_co_u32_e32 v107, vcc, 0, v5, vcc
	v_add_co_u32_e32 v108, vcc, s38, v4
	v_lshlrev_b64 v[50:51], 12, v[50:51]
	s_nop 0
	v_addc_co_u32_e32 v109, vcc, 0, v5, vcc
	v_add_co_u32_e32 v110, vcc, s39, v4
	v_lshlrev_b64 v[52:53], 12, v[52:53]
	s_nop 0
	v_addc_co_u32_e32 v111, vcc, 0, v5, vcc
	v_add_co_u32_e32 v112, vcc, s40, v4
	v_lshlrev_b64 v[54:55], 12, v[54:55]
	s_nop 0
	v_addc_co_u32_e32 v113, vcc, 0, v5, vcc
	v_add_co_u32_e32 v114, vcc, s41, v4
	v_lshl_add_u64 v[120:121], s[10:11], 0, v[2:3]
	s_nop 0
	v_addc_co_u32_e32 v115, vcc, 0, v5, vcc
	v_add_co_u32_e32 v116, vcc, s42, v4
	v_lshl_add_u64 v[122:123], v[120:121], 0, v[40:41]
	s_nop 0
	v_addc_co_u32_e32 v117, vcc, 0, v5, vcc
	v_add_co_u32_e32 v118, vcc, s43, v4
	v_lshl_add_u64 v[124:125], v[120:121], 0, v[42:43]
	s_nop 0
	v_addc_co_u32_e32 v119, vcc, 0, v5, vcc
	global_load_dwordx2 v[4:5], v[4:5], off nt
	s_nop 0
	global_load_dwordx2 v[56:57], v[56:57], off nt
	s_nop 0
	global_load_dwordx2 v[58:59], v[58:59], off nt
	s_nop 0
	global_load_dwordx2 v[60:61], v[60:61], off nt
	s_nop 0
	global_load_dwordx2 v[62:63], v[62:63], off nt
	s_nop 0
	global_load_dwordx2 v[64:65], v[64:65], off nt
	s_nop 0
	global_load_dwordx2 v[66:67], v[66:67], off nt
	s_nop 0
	global_load_dwordx2 v[68:69], v[68:69], off nt
	s_nop 0
	global_load_dwordx2 v[70:71], v[70:71], off nt
	s_nop 0
	global_load_dwordx2 v[72:73], v[72:73], off nt
	s_nop 0
	global_load_dwordx2 v[76:77], v[76:77], off nt
	s_nop 0
	global_load_dwordx2 v[78:79], v[78:79], off nt
	s_nop 0
	global_load_dwordx2 v[80:81], v[80:81], off nt
	s_nop 0
	global_load_dwordx2 v[82:83], v[82:83], off nt
	s_nop 0
	global_load_dwordx2 v[84:85], v[84:85], off nt
	s_nop 0
	global_load_dwordx2 v[86:87], v[86:87], off nt
	s_nop 0
	global_load_dwordx2 v[88:89], v[88:89], off nt
	s_nop 0
	global_load_dwordx2 v[90:91], v[90:91], off nt
	s_nop 0
	global_load_dwordx2 v[92:93], v[92:93], off nt
	s_nop 0
	global_load_dwordx2 v[94:95], v[94:95], off nt
	s_nop 0
	global_load_dwordx2 v[96:97], v[96:97], off nt
	s_nop 0
	global_load_dwordx2 v[98:99], v[98:99], off nt
	s_nop 0
	global_load_dwordx2 v[100:101], v[100:101], off nt
	s_nop 0
	global_load_dwordx2 v[102:103], v[102:103], off nt
	s_nop 0
	global_load_dwordx2 v[104:105], v[104:105], off nt
	s_nop 0
	global_load_dwordx2 v[106:107], v[106:107], off nt
	s_nop 0
	global_load_dwordx2 v[108:109], v[108:109], off nt
	s_nop 0
	global_load_dwordx2 v[110:111], v[110:111], off nt
	s_nop 0
	global_load_dwordx2 v[112:113], v[112:113], off nt
	s_nop 0
	global_load_dwordx2 v[114:115], v[114:115], off nt
	s_nop 0
	global_load_dwordx2 v[116:117], v[116:117], off nt
	s_nop 0
	global_load_dwordx2 v[118:119], v[118:119], off nt
	s_waitcnt vmcnt(0)
	ds_write2_b32 v7, v4, v5 offset1:1
	ds_write2_b32 v7, v56, v57 offset0:130 offset1:131
	ds_write2_b32 v8, v58, v59 offset1:1
	ds_write2_b32 v9, v60, v61 offset1:1
	ds_write2_b32 v10, v62, v63 offset1:1
	ds_write2_b32 v11, v64, v65 offset1:1
	ds_write2_b32 v12, v66, v67 offset1:1
	ds_write2_b32 v13, v68, v69 offset1:1
	ds_write2_b32 v14, v70, v71 offset1:1
	ds_write2_b32 v15, v72, v73 offset1:1
	ds_write2_b32 v16, v76, v77 offset1:1
	ds_write2_b32 v17, v78, v79 offset1:1
	ds_write2_b32 v18, v80, v81 offset1:1
	ds_write2_b32 v19, v82, v83 offset1:1
	ds_write2_b32 v20, v84, v85 offset1:1
	ds_write2_b32 v21, v86, v87 offset1:1
	ds_write2_b32 v22, v88, v89 offset1:1
	ds_write2_b32 v23, v90, v91 offset1:1
	ds_write2_b32 v24, v92, v93 offset1:1
	ds_write2_b32 v25, v94, v95 offset1:1
	ds_write2_b32 v26, v96, v97 offset1:1
	ds_write2_b32 v27, v98, v99 offset1:1
	ds_write2_b32 v28, v100, v101 offset1:1
	ds_write2_b32 v29, v102, v103 offset1:1
	ds_write2_b32 v30, v104, v105 offset1:1
	ds_write2_b32 v31, v106, v107 offset1:1
	ds_write2_b32 v32, v108, v109 offset1:1
	ds_write2_b32 v33, v110, v111 offset1:1
	ds_write2_b32 v34, v112, v113 offset1:1
	ds_write2_b32 v35, v114, v115 offset1:1
	ds_write2_b32 v36, v116, v117 offset1:1
	ds_write2_b32 v37, v118, v119 offset1:1
	s_waitcnt lgkmcnt(0)
	v_lshl_add_u64 v[126:127], v[120:121], 0, v[44:45]
	v_lshl_add_u64 v[128:129], v[120:121], 0, v[46:47]
	v_lshl_add_u64 v[130:131], v[120:121], 0, v[48:49]
	v_lshl_add_u64 v[132:133], v[120:121], 0, v[50:51]
	v_lshl_add_u64 v[134:135], v[120:121], 0, v[52:53]
	v_lshl_add_u64 v[120:121], v[120:121], 0, v[54:55]
	ds_read2_b32 v[4:5], v6 offset0:65 offset1:73
	ds_read2_b32 v[44:45], v6 offset1:8
	ds_read2_b32 v[46:47], v6 offset0:130 offset1:138
	ds_read2_b32 v[48:49], v6 offset0:195 offset1:203
	ds_read2_b32 v[50:51], v38 offset0:4 offset1:12
	ds_read2_b32 v[52:53], v38 offset0:69 offset1:77
	ds_read2_b32 v[54:55], v38 offset0:134 offset1:142
	ds_read2_b32 v[56:57], v38 offset0:199 offset1:207
	ds_read2_b32 v[58:59], v6 offset0:81 offset1:89
	ds_read2_b32 v[60:61], v6 offset0:16 offset1:24
	ds_read2_b32 v[62:63], v6 offset0:146 offset1:154
	ds_read2_b32 v[64:65], v6 offset0:211 offset1:219
	ds_read2_b32 v[66:67], v38 offset0:20 offset1:28
	ds_read2_b32 v[68:69], v38 offset0:85 offset1:93
	ds_read2_b32 v[70:71], v38 offset0:150 offset1:158
	ds_read2_b32 v[72:73], v38 offset0:215 offset1:223
	ds_read2_b32 v[76:77], v6 offset0:32 offset1:40
	ds_read2_b32 v[78:79], v6 offset0:97 offset1:105
	ds_read2_b32 v[80:81], v6 offset0:162 offset1:170
	ds_read2_b32 v[82:83], v6 offset0:227 offset1:235
	ds_read2_b32 v[84:85], v38 offset0:36 offset1:44
	ds_read2_b32 v[86:87], v38 offset0:101 offset1:109
	ds_read2_b32 v[88:89], v38 offset0:166 offset1:174
	ds_read2_b32 v[90:91], v38 offset0:231 offset1:239
	ds_read2_b32 v[92:93], v6 offset0:48 offset1:56
	ds_read2_b32 v[94:95], v6 offset0:113 offset1:121
	ds_read2_b32 v[96:97], v6 offset0:178 offset1:186
	ds_read2_b32 v[98:99], v6 offset0:243 offset1:251
	ds_read2_b32 v[100:101], v38 offset0:52 offset1:60
	ds_read2_b32 v[102:103], v38 offset0:117 offset1:125
	ds_read2_b32 v[104:105], v38 offset0:182 offset1:190
	ds_read2_b32 v[106:107], v38 offset0:247 offset1:255
	s_waitcnt lgkmcnt(14)
	v_cvt_pk_bf16_f32 v40, v44, v4
	v_cvt_pk_bf16_f32 v41, v46, v48
	v_cvt_pk_bf16_f32 v42, v50, v52
	v_cvt_pk_bf16_f32 v43, v54, v56
	v_cvt_pk_bf16_f32 v44, v45, v5
	v_cvt_pk_bf16_f32 v45, v47, v49
	v_cvt_pk_bf16_f32 v46, v51, v53
	v_cvt_pk_bf16_f32 v47, v55, v57
	v_cvt_pk_bf16_f32 v48, v60, v58
	v_cvt_pk_bf16_f32 v49, v62, v64
	v_cvt_pk_bf16_f32 v50, v66, v68
	v_cvt_pk_bf16_f32 v51, v70, v72
	v_cvt_pk_bf16_f32 v52, v61, v59
	v_cvt_pk_bf16_f32 v53, v63, v65
	v_cvt_pk_bf16_f32 v54, v67, v69
	v_cvt_pk_bf16_f32 v55, v71, v73
	v_cvt_pk_bf16_f32 v56, v76, v78
	s_waitcnt lgkmcnt(12)
	v_cvt_pk_bf16_f32 v57, v80, v82
	s_waitcnt lgkmcnt(10)
	v_cvt_pk_bf16_f32 v58, v84, v86
	s_waitcnt lgkmcnt(8)
	v_cvt_pk_bf16_f32 v59, v88, v90
	v_cvt_pk_bf16_f32 v60, v77, v79
	v_cvt_pk_bf16_f32 v61, v81, v83
	v_cvt_pk_bf16_f32 v62, v85, v87
	v_cvt_pk_bf16_f32 v63, v89, v91
	s_waitcnt lgkmcnt(6)
	v_cvt_pk_bf16_f32 v64, v92, v94
	s_waitcnt lgkmcnt(4)
	v_cvt_pk_bf16_f32 v65, v96, v98
	s_waitcnt lgkmcnt(2)
	v_cvt_pk_bf16_f32 v66, v100, v102
	s_waitcnt lgkmcnt(0)
	v_cvt_pk_bf16_f32 v67, v104, v106
	v_cvt_pk_bf16_f32 v68, v93, v95
	v_cvt_pk_bf16_f32 v69, v97, v99
	v_cvt_pk_bf16_f32 v70, v101, v103
	v_cvt_pk_bf16_f32 v71, v105, v107
	global_store_dwordx4 v[122:123], v[40:43], off nt
	global_store_dwordx4 v[124:125], v[44:47], off nt
	global_store_dwordx4 v[126:127], v[48:51], off nt
	global_store_dwordx4 v[128:129], v[52:55], off nt
	global_store_dwordx4 v[130:131], v[56:59], off nt
	global_store_dwordx4 v[132:133], v[60:63], off nt
	global_store_dwordx4 v[134:135], v[64:67], off nt
	global_store_dwordx4 v[120:121], v[68:71], off nt
	s_waitcnt lgkmcnt(0)
	s_addk_i32 s0, 0x400
	s_cmpk_gt_i32 s0, 0x13ff
	s_cbranch_scc0 .LBB0_2219
